# expert-weight conversion groups: packed v_pk_mul scaling in place, no zero-fill moves before the fp8 converts
# speedup vs baseline: 1.0058x; 1.0058x over previous
; #define LAS __attribute__((address_space(3)))
; DI unsigned pk4_fp8(float a, float b, float c, float d) { unsigned p = 0u; p = __builtin_amdgcn_cvt_pk_fp8_f32(f8clamp(a), f8clamp(b), p, false); p = __builtin_amdgcn_cvt_pk_fp8_f32(f8clamp(c), f8clamp(d), p, true); return p; }
; DI float f8clamp(float x) { return __builtin_amdgcn_fmed3f(x, -448.f, 448.f); }
; DI void f8_convert_reload(f32x4 (&v)[4][4], int hb, float sc, LAS unsigned char* scr, bool reload, const F8Tile& dn, int lane) {
;     const int nq = lane & 15, kq = lane >> 4;
; #pragma unroll
;     for (int it = 0; it < 4; ++it) {
; #pragma unroll
;         for (int i = 0; i < 4; ++i) *(LAS unsigned*)(scr + (4 * nq + i) * 132 + hb * 64 + it * 16 + kq * 4) = pk4_fp8(v[it][0][i] * sc, v[it][1][i] * sc, v[it][2][i] * sc, v[it][3][i] * sc);
;         if (reload) {
; #pragma unroll
;             for (int j = 0; j < 4; ++j) v[it][j] = __builtin_nontemporal_load((const f32x4*)(dn.W + (size_t)(dn.k0 + hb * 64 + it * 16 + kq * 4 + j) * dn.N + dn.n0 + 4 * nq)); } }
; }
.Lcvw1:
	s_waitcnt vmcnt(28)
	s_mov_b32 s30, 0x42800000
	s_mov_b32 s31, 0x42800000
	v_pk_mul_f32 v[114:115], v[114:115], s[30:31]
	v_pk_mul_f32 v[116:117], v[116:117], s[30:31]
	v_pk_mul_f32 v[118:119], v[118:119], s[30:31]
	v_pk_mul_f32 v[120:121], v[120:121], s[30:31]
	v_pk_mul_f32 v[122:123], v[122:123], s[30:31]
	v_pk_mul_f32 v[124:125], v[124:125], s[30:31]
	v_pk_mul_f32 v[126:127], v[126:127], s[30:31]
	v_pk_mul_f32 v[128:129], v[128:129], s[30:31]
	v_med3_f32 v114, v114, s25, v189
	v_med3_f32 v115, v115, s25, v189
	v_med3_f32 v116, v116, s25, v189
	v_med3_f32 v117, v117, s25, v189
	v_med3_f32 v118, v118, s25, v189
	v_med3_f32 v119, v119, s25, v189
	v_med3_f32 v120, v120, s25, v189
	v_med3_f32 v121, v121, s25, v189
	v_med3_f32 v122, v122, s25, v189
	v_med3_f32 v123, v123, s25, v189
	v_med3_f32 v124, v124, s25, v189
	v_med3_f32 v125, v125, s25, v189
	v_med3_f32 v126, v126, s25, v189
	v_med3_f32 v127, v127, s25, v189
	v_med3_f32 v128, v128, s25, v189
	v_med3_f32 v129, v129, s25, v189
	v_cvt_pk_fp8_f32 v193, v118, v114
	v_cvt_pk_fp8_f32 v193, v126, v122 op_sel:[0,0,1]
	v_cvt_pk_fp8_f32 v194, v119, v115
	v_cvt_pk_fp8_f32 v194, v127, v123 op_sel:[0,0,1]
	v_cvt_pk_fp8_f32 v195, v120, v116
	v_cvt_pk_fp8_f32 v195, v128, v124 op_sel:[0,0,1]
	v_cvt_pk_fp8_f32 v196, v121, v117
	v_cvt_pk_fp8_f32 v196, v129, v125 op_sel:[0,0,1]
	v_cndmask_b32_e64 v134, 0, 1, s[16:17]
	v_cmp_ne_u32_e64 s[2:3], 1, v134
	s_andn2_b64 vcc, exec, s[16:17]
	v_lshlrev_b32_e32 v134, 2, v132
	ds_write2_b32 v190, v193, v194 offset1:33
	ds_write2_b32 v190, v195, v196 offset0:66 offset1:99
	s_cbranch_vccnz .LBB0_154
	s_mul_i32 s30, s27, s18
	s_add_i32 s30, s30, s4
	s_lshl_b32 s30, s30, 2
	s_add_u32 s16, s8, s30
	s_addc_u32 s17, s9, 0
	s_lshl_b32 s31, s18, 2
	v_mad_u32_u24 v118, v1, s31, v134
	v_mad_u32_u24 v114, v133, s31, v134
	v_mad_u32_u24 v126, v158, s31, v134
	v_mad_u32_u24 v122, v159, s31, v134
	global_load_dwordx4 v[118:121], v118, s[16:17] nt
	global_load_dwordx4 v[114:117], v114, s[16:17] nt
	global_load_dwordx4 v[126:129], v126, s[16:17] nt
	global_load_dwordx4 v[122:125], v122, s[16:17] nt
.LBB0_154:
	s_waitcnt vmcnt(28)
	s_mov_b32 s30, 0x42800000
	s_mov_b32 s31, 0x42800000
	v_pk_mul_f32 v[98:99], v[98:99], s[30:31]
	v_pk_mul_f32 v[100:101], v[100:101], s[30:31]
	v_pk_mul_f32 v[102:103], v[102:103], s[30:31]
	v_pk_mul_f32 v[104:105], v[104:105], s[30:31]
	v_pk_mul_f32 v[106:107], v[106:107], s[30:31]
	v_pk_mul_f32 v[108:109], v[108:109], s[30:31]
	v_pk_mul_f32 v[110:111], v[110:111], s[30:31]
	v_pk_mul_f32 v[112:113], v[112:113], s[30:31]
	v_med3_f32 v98, v98, s25, v189
	v_med3_f32 v99, v99, s25, v189
	v_med3_f32 v100, v100, s25, v189
	v_med3_f32 v101, v101, s25, v189
	v_med3_f32 v102, v102, s25, v189
	v_med3_f32 v103, v103, s25, v189
	v_med3_f32 v104, v104, s25, v189
	v_med3_f32 v105, v105, s25, v189
	v_med3_f32 v106, v106, s25, v189
	v_med3_f32 v107, v107, s25, v189
	v_med3_f32 v108, v108, s25, v189
	v_med3_f32 v109, v109, s25, v189
	v_med3_f32 v110, v110, s25, v189
	v_med3_f32 v111, v111, s25, v189
	v_med3_f32 v112, v112, s25, v189
	v_med3_f32 v113, v113, s25, v189
	v_cvt_pk_fp8_f32 v194, v102, v98
	v_cvt_pk_fp8_f32 v194, v110, v106 op_sel:[0,0,1]
	v_cvt_pk_fp8_f32 v195, v103, v99
	v_cvt_pk_fp8_f32 v195, v111, v107 op_sel:[0,0,1]
	v_cvt_pk_fp8_f32 v196, v104, v100
	v_cvt_pk_fp8_f32 v196, v112, v108 op_sel:[0,0,1]
	v_cvt_pk_fp8_f32 v197, v105, v101
	v_cvt_pk_fp8_f32 v197, v113, v109 op_sel:[0,0,1]
	s_and_b64 vcc, exec, s[2:3]
	ds_write2_b32 v190, v194, v195 offset0:4 offset1:37
	ds_write2_b32 v190, v196, v197 offset0:70 offset1:103
	s_cbranch_vccnz .LBB0_156
	s_mul_i32 s30, s27, s18
	s_add_i32 s30, s30, s4
	s_lshl_b32 s30, s30, 2
	s_add_u32 s16, s8, s30
	s_addc_u32 s17, s9, 0
	s_lshl_b32 s31, s18, 2
	v_mad_u32_u24 v102, v160, s31, v134
	v_mad_u32_u24 v98, v161, s31, v134
	v_mad_u32_u24 v110, v162, s31, v134
	v_mad_u32_u24 v106, v163, s31, v134
	global_load_dwordx4 v[102:105], v102, s[16:17] nt
	global_load_dwordx4 v[98:101], v98, s[16:17] nt
	global_load_dwordx4 v[110:113], v110, s[16:17] nt
	global_load_dwordx4 v[106:109], v106, s[16:17] nt
.LBB0_156:
	s_waitcnt vmcnt(28)
	s_mov_b32 s30, 0x42800000
	s_mov_b32 s31, 0x42800000
	v_pk_mul_f32 v[82:83], v[82:83], s[30:31]
	v_pk_mul_f32 v[84:85], v[84:85], s[30:31]
	v_pk_mul_f32 v[86:87], v[86:87], s[30:31]
	v_pk_mul_f32 v[88:89], v[88:89], s[30:31]
	v_pk_mul_f32 v[90:91], v[90:91], s[30:31]
	v_pk_mul_f32 v[92:93], v[92:93], s[30:31]
	v_pk_mul_f32 v[94:95], v[94:95], s[30:31]
	v_pk_mul_f32 v[96:97], v[96:97], s[30:31]
	v_med3_f32 v82, v82, s25, v189
	v_med3_f32 v83, v83, s25, v189
	v_med3_f32 v84, v84, s25, v189
	v_med3_f32 v85, v85, s25, v189
	v_med3_f32 v86, v86, s25, v189
	v_med3_f32 v87, v87, s25, v189
	v_med3_f32 v88, v88, s25, v189
	v_med3_f32 v89, v89, s25, v189
	v_med3_f32 v90, v90, s25, v189
	v_med3_f32 v91, v91, s25, v189
	v_med3_f32 v92, v92, s25, v189
	v_med3_f32 v93, v93, s25, v189
	v_med3_f32 v94, v94, s25, v189
	v_med3_f32 v95, v95, s25, v189
	v_med3_f32 v96, v96, s25, v189
	v_med3_f32 v97, v97, s25, v189
	v_cvt_pk_fp8_f32 v194, v86, v82
	v_cvt_pk_fp8_f32 v194, v94, v90 op_sel:[0,0,1]
	v_cvt_pk_fp8_f32 v195, v87, v83
	v_cvt_pk_fp8_f32 v195, v95, v91 op_sel:[0,0,1]
	v_cvt_pk_fp8_f32 v196, v88, v84
	v_cvt_pk_fp8_f32 v196, v96, v92 op_sel:[0,0,1]
	v_cvt_pk_fp8_f32 v197, v89, v85
	v_cvt_pk_fp8_f32 v197, v97, v93 op_sel:[0,0,1]
	s_and_b64 vcc, exec, s[2:3]
	ds_write2_b32 v190, v194, v195 offset0:8 offset1:41
	ds_write2_b32 v190, v196, v197 offset0:74 offset1:107
	s_cbranch_vccnz .LBB0_158
	s_mul_i32 s30, s27, s18
	s_add_i32 s30, s30, s4
	s_lshl_b32 s30, s30, 2
	s_add_u32 s16, s8, s30
	s_addc_u32 s17, s9, 0
	s_lshl_b32 s31, s18, 2
	v_mad_u32_u24 v86, v164, s31, v134
	v_mad_u32_u24 v82, v165, s31, v134
	v_mad_u32_u24 v94, v166, s31, v134
	v_mad_u32_u24 v90, v167, s31, v134
	global_load_dwordx4 v[86:89], v86, s[16:17] nt
	global_load_dwordx4 v[82:85], v82, s[16:17] nt
	global_load_dwordx4 v[94:97], v94, s[16:17] nt
	global_load_dwordx4 v[90:93], v90, s[16:17] nt
; #define LAS __attribute__((address_space(3)))
; DI unsigned pk4_fp8(float a, float b, float c, float d) { unsigned p = 0u; p = __builtin_amdgcn_cvt_pk_fp8_f32(f8clamp(a), f8clamp(b), p, false); p = __builtin_amdgcn_cvt_pk_fp8_f32(f8clamp(c), f8clamp(d), p, true); return p; }
; DI float f8clamp(float x) { return __builtin_amdgcn_fmed3f(x, -448.f, 448.f); }
; DI void f8_convert_reload(f32x4 (&v)[4][4], int hb, float sc, LAS unsigned char* scr, bool reload, const F8Tile& dn, int lane) {
;     const int nq = lane & 15, kq = lane >> 4;
; #pragma unroll
;     for (int it = 0; it < 4; ++it) {
; #pragma unroll
;         for (int i = 0; i < 4; ++i) *(LAS unsigned*)(scr + (4 * nq + i) * 132 + hb * 64 + it * 16 + kq * 4) = pk4_fp8(v[it][0][i] * sc, v[it][1][i] * sc, v[it][2][i] * sc, v[it][3][i] * sc);
;         if (reload) {
; #pragma unroll
;             for (int j = 0; j < 4; ++j) v[it][j] = __builtin_nontemporal_load((const f32x4*)(dn.W + (size_t)(dn.k0 + hb * 64 + it * 16 + kq * 4 + j) * dn.N + dn.n0 + 4 * nq)); } }
; }
.LBB0_158:
	s_waitcnt vmcnt(28)
	s_mov_b32 s30, 0x42800000
	s_mov_b32 s31, 0x42800000
	v_pk_mul_f32 v[66:67], v[66:67], s[30:31]
	v_pk_mul_f32 v[68:69], v[68:69], s[30:31]
	v_pk_mul_f32 v[70:71], v[70:71], s[30:31]
	v_pk_mul_f32 v[72:73], v[72:73], s[30:31]
	v_pk_mul_f32 v[74:75], v[74:75], s[30:31]
	v_pk_mul_f32 v[76:77], v[76:77], s[30:31]
	v_pk_mul_f32 v[78:79], v[78:79], s[30:31]
	v_pk_mul_f32 v[80:81], v[80:81], s[30:31]
	v_med3_f32 v66, v66, s25, v189
	v_med3_f32 v67, v67, s25, v189
	v_med3_f32 v68, v68, s25, v189
	v_med3_f32 v69, v69, s25, v189
	v_med3_f32 v70, v70, s25, v189
	v_med3_f32 v71, v71, s25, v189
	v_med3_f32 v72, v72, s25, v189
	v_med3_f32 v73, v73, s25, v189
	v_med3_f32 v74, v74, s25, v189
	v_med3_f32 v75, v75, s25, v189
	v_med3_f32 v76, v76, s25, v189
	v_med3_f32 v77, v77, s25, v189
	v_med3_f32 v78, v78, s25, v189
	v_med3_f32 v79, v79, s25, v189
	v_med3_f32 v80, v80, s25, v189
	v_med3_f32 v81, v81, s25, v189
	v_cvt_pk_fp8_f32 v194, v70, v66
	v_cvt_pk_fp8_f32 v194, v74, v78 op_sel:[0,0,1]
	v_cvt_pk_fp8_f32 v195, v71, v67
	v_cvt_pk_fp8_f32 v195, v75, v79 op_sel:[0,0,1]
	v_cvt_pk_fp8_f32 v196, v72, v68
	v_cvt_pk_fp8_f32 v196, v76, v80 op_sel:[0,0,1]
	v_cvt_pk_fp8_f32 v197, v73, v69
	v_cvt_pk_fp8_f32 v197, v77, v81 op_sel:[0,0,1]
	s_and_b64 vcc, exec, s[2:3]
	ds_write2_b32 v190, v194, v195 offset0:12 offset1:45
	ds_write2_b32 v190, v196, v197 offset0:78 offset1:111
	s_cbranch_vccnz .LBB0_160
	s_mul_i32 s30, s27, s18
	s_add_i32 s30, s30, s4
	s_lshl_b32 s30, s30, 2
	s_add_u32 s16, s8, s30
	s_addc_u32 s17, s9, 0
	s_lshl_b32 s31, s18, 2
	v_mad_u32_u24 v70, v168, s31, v134
	v_mad_u32_u24 v66, v169, s31, v134
	v_mad_u32_u24 v74, v170, s31, v134
	v_mad_u32_u24 v78, v171, s31, v134
	global_load_dwordx4 v[70:73], v70, s[16:17] nt
	global_load_dwordx4 v[66:69], v66, s[16:17] nt
	global_load_dwordx4 v[74:77], v74, s[16:17] nt
	global_load_dwordx4 v[78:81], v78, s[16:17] nt
.LBB0_160:
	s_waitcnt vmcnt(28)
	s_mov_b32 s30, 0x42800000
	s_mov_b32 s31, 0x42800000
	v_pk_mul_f32 v[50:51], v[50:51], s[30:31]
	v_pk_mul_f32 v[52:53], v[52:53], s[30:31]
	v_pk_mul_f32 v[54:55], v[54:55], s[30:31]
	v_pk_mul_f32 v[56:57], v[56:57], s[30:31]
	v_pk_mul_f32 v[58:59], v[58:59], s[30:31]
	v_pk_mul_f32 v[60:61], v[60:61], s[30:31]
	v_pk_mul_f32 v[62:63], v[62:63], s[30:31]
	v_pk_mul_f32 v[64:65], v[64:65], s[30:31]
	v_med3_f32 v50, v50, s25, v189
	v_med3_f32 v51, v51, s25, v189
	v_med3_f32 v52, v52, s25, v189
	v_med3_f32 v53, v53, s25, v189
	v_med3_f32 v54, v54, s25, v189
	v_med3_f32 v55, v55, s25, v189
	v_med3_f32 v56, v56, s25, v189
	v_med3_f32 v57, v57, s25, v189
	v_med3_f32 v58, v58, s25, v189
	v_med3_f32 v59, v59, s25, v189
	v_med3_f32 v60, v60, s25, v189
	v_med3_f32 v61, v61, s25, v189
	v_med3_f32 v62, v62, s25, v189
	v_med3_f32 v63, v63, s25, v189
	v_med3_f32 v64, v64, s25, v189
	v_med3_f32 v65, v65, s25, v189
	v_cvt_pk_fp8_f32 v194, v54, v50
	v_cvt_pk_fp8_f32 v194, v62, v58 op_sel:[0,0,1]
	v_cvt_pk_fp8_f32 v195, v55, v51
	v_cvt_pk_fp8_f32 v195, v63, v59 op_sel:[0,0,1]
	v_cvt_pk_fp8_f32 v196, v56, v52
	v_cvt_pk_fp8_f32 v196, v64, v60 op_sel:[0,0,1]
	v_cvt_pk_fp8_f32 v197, v57, v53
	v_cvt_pk_fp8_f32 v197, v65, v61 op_sel:[0,0,1]
	s_and_b64 vcc, exec, s[2:3]
	ds_write2_b32 v190, v194, v195 offset0:16 offset1:49
	ds_write2_b32 v190, v196, v197 offset0:82 offset1:115
	s_cbranch_vccnz .LBB0_162
	s_mul_i32 s30, s27, s18
	s_add_i32 s30, s30, s4
	s_lshl_b32 s30, s30, 2
	s_add_u32 s16, s8, s30
	s_addc_u32 s17, s9, 0
	s_lshl_b32 s31, s18, 2
	v_mad_u32_u24 v54, v172, s31, v134
	v_mad_u32_u24 v50, v173, s31, v134
	v_mad_u32_u24 v62, v174, s31, v134
	v_mad_u32_u24 v58, v175, s31, v134
	global_load_dwordx4 v[54:57], v54, s[16:17] nt
	global_load_dwordx4 v[50:53], v50, s[16:17] nt
	global_load_dwordx4 v[62:65], v62, s[16:17] nt
	global_load_dwordx4 v[58:61], v58, s[16:17] nt
; #define LAS __attribute__((address_space(3)))
; DI unsigned pk4_fp8(float a, float b, float c, float d) { unsigned p = 0u; p = __builtin_amdgcn_cvt_pk_fp8_f32(f8clamp(a), f8clamp(b), p, false); p = __builtin_amdgcn_cvt_pk_fp8_f32(f8clamp(c), f8clamp(d), p, true); return p; }
; DI float f8clamp(float x) { return __builtin_amdgcn_fmed3f(x, -448.f, 448.f); }
; DI void f8_convert_reload(f32x4 (&v)[4][4], int hb, float sc, LAS unsigned char* scr, bool reload, const F8Tile& dn, int lane) {
;     const int nq = lane & 15, kq = lane >> 4;
; #pragma unroll
;     for (int it = 0; it < 4; ++it) {
; #pragma unroll
;         for (int i = 0; i < 4; ++i) *(LAS unsigned*)(scr + (4 * nq + i) * 132 + hb * 64 + it * 16 + kq * 4) = pk4_fp8(v[it][0][i] * sc, v[it][1][i] * sc, v[it][2][i] * sc, v[it][3][i] * sc);
;         if (reload) {
; #pragma unroll
;             for (int j = 0; j < 4; ++j) v[it][j] = __builtin_nontemporal_load((const f32x4*)(dn.W + (size_t)(dn.k0 + hb * 64 + it * 16 + kq * 4 + j) * dn.N + dn.n0 + 4 * nq)); } }
; }
.LBB0_162:
	s_waitcnt vmcnt(28)
	s_mov_b32 s30, 0x42800000
	s_mov_b32 s31, 0x42800000
	v_pk_mul_f32 v[34:35], v[34:35], s[30:31]
	v_pk_mul_f32 v[36:37], v[36:37], s[30:31]
	v_pk_mul_f32 v[38:39], v[38:39], s[30:31]
	v_pk_mul_f32 v[40:41], v[40:41], s[30:31]
	v_pk_mul_f32 v[42:43], v[42:43], s[30:31]
	v_pk_mul_f32 v[44:45], v[44:45], s[30:31]
	v_pk_mul_f32 v[46:47], v[46:47], s[30:31]
	v_pk_mul_f32 v[48:49], v[48:49], s[30:31]
	v_med3_f32 v34, v34, s25, v189
	v_med3_f32 v35, v35, s25, v189
	v_med3_f32 v36, v36, s25, v189
	v_med3_f32 v37, v37, s25, v189
	v_med3_f32 v38, v38, s25, v189
	v_med3_f32 v39, v39, s25, v189
	v_med3_f32 v40, v40, s25, v189
	v_med3_f32 v41, v41, s25, v189
	v_med3_f32 v42, v42, s25, v189
	v_med3_f32 v43, v43, s25, v189
	v_med3_f32 v44, v44, s25, v189
	v_med3_f32 v45, v45, s25, v189
	v_med3_f32 v46, v46, s25, v189
	v_med3_f32 v47, v47, s25, v189
	v_med3_f32 v48, v48, s25, v189
	v_med3_f32 v49, v49, s25, v189
	v_cvt_pk_fp8_f32 v194, v38, v34
	v_cvt_pk_fp8_f32 v194, v46, v42 op_sel:[0,0,1]
	v_cvt_pk_fp8_f32 v195, v39, v35
	v_cvt_pk_fp8_f32 v195, v47, v43 op_sel:[0,0,1]
	v_cvt_pk_fp8_f32 v196, v40, v36
	v_cvt_pk_fp8_f32 v196, v48, v44 op_sel:[0,0,1]
	v_cvt_pk_fp8_f32 v197, v41, v37
	v_cvt_pk_fp8_f32 v197, v49, v45 op_sel:[0,0,1]
	s_and_b64 vcc, exec, s[2:3]
	ds_write2_b32 v190, v194, v195 offset0:20 offset1:53
	ds_write2_b32 v190, v196, v197 offset0:86 offset1:119
	s_cbranch_vccnz .LBB0_164
	s_mul_i32 s30, s27, s18
	s_add_i32 s30, s30, s4
	s_lshl_b32 s30, s30, 2
	s_add_u32 s16, s8, s30
	s_addc_u32 s17, s9, 0
	s_lshl_b32 s31, s18, 2
	v_mad_u32_u24 v38, v176, s31, v134
	v_mad_u32_u24 v34, v177, s31, v134
	v_mad_u32_u24 v46, v178, s31, v134
	v_mad_u32_u24 v42, v179, s31, v134
	global_load_dwordx4 v[38:41], v38, s[16:17] nt
	global_load_dwordx4 v[34:37], v34, s[16:17] nt
	global_load_dwordx4 v[46:49], v46, s[16:17] nt
	global_load_dwordx4 v[42:45], v42, s[16:17] nt
.LBB0_164:
	s_waitcnt vmcnt(28)
	s_mov_b32 s30, 0x42800000
	s_mov_b32 s31, 0x42800000
	v_pk_mul_f32 v[18:19], v[18:19], s[30:31]
	v_pk_mul_f32 v[20:21], v[20:21], s[30:31]
	v_pk_mul_f32 v[22:23], v[22:23], s[30:31]
	v_pk_mul_f32 v[24:25], v[24:25], s[30:31]
	v_pk_mul_f32 v[26:27], v[26:27], s[30:31]
	v_pk_mul_f32 v[28:29], v[28:29], s[30:31]
	v_pk_mul_f32 v[30:31], v[30:31], s[30:31]
	v_pk_mul_f32 v[32:33], v[32:33], s[30:31]
	v_med3_f32 v18, v18, s25, v189
	v_med3_f32 v19, v19, s25, v189
	v_med3_f32 v20, v20, s25, v189
	v_med3_f32 v21, v21, s25, v189
	v_med3_f32 v22, v22, s25, v189
	v_med3_f32 v23, v23, s25, v189
	v_med3_f32 v24, v24, s25, v189
	v_med3_f32 v25, v25, s25, v189
	v_med3_f32 v26, v26, s25, v189
	v_med3_f32 v27, v27, s25, v189
	v_med3_f32 v28, v28, s25, v189
	v_med3_f32 v29, v29, s25, v189
	v_med3_f32 v30, v30, s25, v189
	v_med3_f32 v31, v31, s25, v189
	v_med3_f32 v32, v32, s25, v189
	v_med3_f32 v33, v33, s25, v189
	v_cvt_pk_fp8_f32 v194, v22, v18
	v_cvt_pk_fp8_f32 v194, v30, v26 op_sel:[0,0,1]
	v_cvt_pk_fp8_f32 v195, v23, v19
	v_cvt_pk_fp8_f32 v195, v31, v27 op_sel:[0,0,1]
	v_cvt_pk_fp8_f32 v196, v24, v20
	v_cvt_pk_fp8_f32 v196, v32, v28 op_sel:[0,0,1]
	v_cvt_pk_fp8_f32 v197, v25, v21
	v_cvt_pk_fp8_f32 v197, v33, v29 op_sel:[0,0,1]
	s_and_b64 vcc, exec, s[2:3]
	ds_write2_b32 v190, v194, v195 offset0:24 offset1:57
	ds_write2_b32 v190, v196, v197 offset0:90 offset1:123
	s_cbranch_vccnz .LBB0_166
	s_mul_i32 s30, s27, s18
	s_add_i32 s30, s30, s4
	s_lshl_b32 s30, s30, 2
	s_add_u32 s16, s8, s30
	s_addc_u32 s17, s9, 0
	s_lshl_b32 s31, s18, 2
	v_mad_u32_u24 v22, v180, s31, v134
	v_mad_u32_u24 v18, v181, s31, v134
	v_mad_u32_u24 v30, v182, s31, v134
	v_mad_u32_u24 v26, v183, s31, v134
	global_load_dwordx4 v[22:25], v22, s[16:17] nt
	global_load_dwordx4 v[18:21], v18, s[16:17] nt
	global_load_dwordx4 v[30:33], v30, s[16:17] nt
	global_load_dwordx4 v[26:29], v26, s[16:17] nt
.LBB0_166:
	s_waitcnt vmcnt(28)
	s_mov_b32 s16, 0x42800000
	s_mov_b32 s17, 0x42800000
	v_pk_mul_f32 v[2:3], v[2:3], s[16:17]
	v_pk_mul_f32 v[4:5], v[4:5], s[16:17]
	v_pk_mul_f32 v[6:7], v[6:7], s[16:17]
	v_pk_mul_f32 v[8:9], v[8:9], s[16:17]
	v_pk_mul_f32 v[10:11], v[10:11], s[16:17]
	v_pk_mul_f32 v[12:13], v[12:13], s[16:17]
	v_pk_mul_f32 v[14:15], v[14:15], s[16:17]
	v_pk_mul_f32 v[16:17], v[16:17], s[16:17]
	v_med3_f32 v2, v2, s25, v189
	v_med3_f32 v3, v3, s25, v189
	v_med3_f32 v4, v4, s25, v189
	v_med3_f32 v5, v5, s25, v189
	v_med3_f32 v6, v6, s25, v189
	v_med3_f32 v7, v7, s25, v189
	v_med3_f32 v8, v8, s25, v189
	v_med3_f32 v9, v9, s25, v189
	v_med3_f32 v10, v10, s25, v189
	v_med3_f32 v11, v11, s25, v189
	v_med3_f32 v12, v12, s25, v189
	v_med3_f32 v13, v13, s25, v189
	v_med3_f32 v14, v14, s25, v189
	v_med3_f32 v15, v15, s25, v189
	v_med3_f32 v16, v16, s25, v189
	v_med3_f32 v17, v17, s25, v189
	v_cvt_pk_fp8_f32 v194, v6, v2
	v_cvt_pk_fp8_f32 v194, v14, v10 op_sel:[0,0,1]
	v_cvt_pk_fp8_f32 v195, v7, v3
	v_cvt_pk_fp8_f32 v195, v15, v11 op_sel:[0,0,1]
	v_cvt_pk_fp8_f32 v196, v8, v4
	v_cvt_pk_fp8_f32 v196, v16, v12 op_sel:[0,0,1]
	v_cvt_pk_fp8_f32 v197, v9, v5
	v_cvt_pk_fp8_f32 v197, v17, v13 op_sel:[0,0,1]
	s_and_b64 vcc, exec, s[2:3]
	ds_write2_b32 v190, v194, v195 offset0:28 offset1:61
	ds_write2_b32 v190, v196, v197 offset0:94 offset1:127
	s_cbranch_vccnz .LBB0_144
	s_mul_i32 s16, s27, s18
	s_add_i32 s16, s16, s4
	s_lshl_b32 s16, s16, 2
	s_add_u32 s2, s8, s16
	s_addc_u32 s3, s9, 0
	s_lshl_b32 s17, s18, 2
	v_mad_u32_u24 v6, v184, s17, v134
	v_mad_u32_u24 v2, v185, s17, v134
	v_mad_u32_u24 v14, v186, s17, v134
	v_mad_u32_u24 v10, v187, s17, v134
	global_load_dwordx4 v[6:9], v6, s[2:3] nt
	global_load_dwordx4 v[2:5], v2, s[2:3] nt
	global_load_dwordx4 v[14:17], v14, s[2:3] nt
	global_load_dwordx4 v[10:13], v10, s[2:3] nt
	s_branch .LBB0_144

; #define LAS __attribute__((address_space(3)))
; DI unsigned pk4_fp8(float a, float b, float c, float d) { unsigned p = 0u; p = __builtin_amdgcn_cvt_pk_fp8_f32(f8clamp(a), f8clamp(b), p, false); p = __builtin_amdgcn_cvt_pk_fp8_f32(f8clamp(c), f8clamp(d), p, true); return p; }
; DI float f8clamp(float x) { return __builtin_amdgcn_fmed3f(x, -448.f, 448.f); }
; DI void f8_convert_reload(f32x4 (&v)[4][4], int hb, float sc, LAS unsigned char* scr, bool reload, const F8Tile& dn, int lane) {
;     const int nq = lane & 15, kq = lane >> 4;
; #pragma unroll
;     for (int it = 0; it < 4; ++it) {
; #pragma unroll
;         for (int i = 0; i < 4; ++i) *(LAS unsigned*)(scr + (4 * nq + i) * 132 + hb * 64 + it * 16 + kq * 4) = pk4_fp8(v[it][0][i] * sc, v[it][1][i] * sc, v[it][2][i] * sc, v[it][3][i] * sc);
;         if (reload) {
; #pragma unroll
;             for (int j = 0; j < 4; ++j) v[it][j] = __builtin_nontemporal_load((const f32x4*)(dn.W + (size_t)(dn.k0 + hb * 64 + it * 16 + kq * 4 + j) * dn.N + dn.n0 + 4 * nq)); } }
; }
.Lcvw2:
	s_waitcnt vmcnt(28)
	s_mov_b32 s28, 0x42800000
	s_mov_b32 s29, 0x42800000
	v_pk_mul_f32 v[114:115], v[114:115], s[28:29]
	v_pk_mul_f32 v[116:117], v[116:117], s[28:29]
	v_pk_mul_f32 v[118:119], v[118:119], s[28:29]
	v_pk_mul_f32 v[120:121], v[120:121], s[28:29]
	v_pk_mul_f32 v[122:123], v[122:123], s[28:29]
	v_pk_mul_f32 v[124:125], v[124:125], s[28:29]
	v_pk_mul_f32 v[126:127], v[126:127], s[28:29]
	v_pk_mul_f32 v[128:129], v[128:129], s[28:29]
	v_med3_f32 v114, v114, s24, v190
	v_med3_f32 v115, v115, s24, v190
	v_med3_f32 v116, v116, s24, v190
	v_med3_f32 v117, v117, s24, v190
	v_med3_f32 v118, v118, s24, v190
	v_med3_f32 v119, v119, s24, v190
	v_med3_f32 v120, v120, s24, v190
	v_med3_f32 v121, v121, s24, v190
	v_med3_f32 v122, v122, s24, v190
	v_med3_f32 v123, v123, s24, v190
	v_med3_f32 v124, v124, s24, v190
	v_med3_f32 v125, v125, s24, v190
	v_med3_f32 v126, v126, s24, v190
	v_med3_f32 v127, v127, s24, v190
	v_med3_f32 v128, v128, s24, v190
	v_med3_f32 v129, v129, s24, v190
	v_cvt_pk_fp8_f32 v194, v118, v114
	v_cvt_pk_fp8_f32 v194, v126, v122 op_sel:[0,0,1]
	v_cvt_pk_fp8_f32 v195, v119, v115
	v_cvt_pk_fp8_f32 v195, v127, v123 op_sel:[0,0,1]
	v_cvt_pk_fp8_f32 v196, v120, v116
	v_cvt_pk_fp8_f32 v196, v128, v124 op_sel:[0,0,1]
	v_cvt_pk_fp8_f32 v197, v121, v117
	v_cvt_pk_fp8_f32 v197, v129, v125 op_sel:[0,0,1]
	v_cndmask_b32_e64 v134, 0, 1, s[14:15]
	v_cmp_ne_u32_e64 s[2:3], 1, v134
	s_andn2_b64 vcc, exec, s[14:15]
	v_lshlrev_b32_e32 v134, 2, v132
	ds_write2_b32 v191, v194, v195 offset1:33
	ds_write2_b32 v191, v196, v197 offset0:66 offset1:99
	s_cbranch_vccnz .LBB0_1356
	s_mul_i32 s28, s26, s16
	s_add_i32 s28, s28, s0
	s_lshl_b32 s28, s28, 2
	s_add_u32 s14, s6, s28
	s_addc_u32 s15, s7, 0
	s_lshl_b32 s29, s16, 2
	v_mad_u32_u24 v118, v1, s29, v134
	v_mad_u32_u24 v114, v133, s29, v134
	v_mad_u32_u24 v126, v158, s29, v134
	v_mad_u32_u24 v122, v159, s29, v134
	global_load_dwordx4 v[118:121], v118, s[14:15] nt
	global_load_dwordx4 v[114:117], v114, s[14:15] nt
	global_load_dwordx4 v[126:129], v126, s[14:15] nt
	global_load_dwordx4 v[122:125], v122, s[14:15] nt
.LBB0_1356:
	s_waitcnt vmcnt(28)
	s_mov_b32 s28, 0x42800000
	s_mov_b32 s29, 0x42800000
	v_pk_mul_f32 v[98:99], v[98:99], s[28:29]
	v_pk_mul_f32 v[100:101], v[100:101], s[28:29]
	v_pk_mul_f32 v[102:103], v[102:103], s[28:29]
	v_pk_mul_f32 v[104:105], v[104:105], s[28:29]
	v_pk_mul_f32 v[106:107], v[106:107], s[28:29]
	v_pk_mul_f32 v[108:109], v[108:109], s[28:29]
	v_pk_mul_f32 v[110:111], v[110:111], s[28:29]
	v_pk_mul_f32 v[112:113], v[112:113], s[28:29]
	v_med3_f32 v98, v98, s24, v190
	v_med3_f32 v99, v99, s24, v190
	v_med3_f32 v100, v100, s24, v190
	v_med3_f32 v101, v101, s24, v190
	v_med3_f32 v102, v102, s24, v190
	v_med3_f32 v103, v103, s24, v190
	v_med3_f32 v104, v104, s24, v190
	v_med3_f32 v105, v105, s24, v190
	v_med3_f32 v106, v106, s24, v190
	v_med3_f32 v107, v107, s24, v190
	v_med3_f32 v108, v108, s24, v190
	v_med3_f32 v109, v109, s24, v190
	v_med3_f32 v110, v110, s24, v190
	v_med3_f32 v111, v111, s24, v190
	v_med3_f32 v112, v112, s24, v190
	v_med3_f32 v113, v113, s24, v190
	v_cvt_pk_fp8_f32 v195, v102, v98
	v_cvt_pk_fp8_f32 v195, v110, v106 op_sel:[0,0,1]
	v_cvt_pk_fp8_f32 v196, v103, v99
	v_cvt_pk_fp8_f32 v196, v111, v107 op_sel:[0,0,1]
	v_cvt_pk_fp8_f32 v197, v104, v100
	v_cvt_pk_fp8_f32 v197, v112, v108 op_sel:[0,0,1]
	v_cvt_pk_fp8_f32 v198, v105, v101
	v_cvt_pk_fp8_f32 v198, v113, v109 op_sel:[0,0,1]
	s_and_b64 vcc, exec, s[2:3]
	ds_write2_b32 v191, v195, v196 offset0:4 offset1:37
	ds_write2_b32 v191, v197, v198 offset0:70 offset1:103
	s_cbranch_vccnz .LBB0_1358
	s_mul_i32 s28, s26, s16
	s_add_i32 s28, s28, s0
	s_lshl_b32 s28, s28, 2
	s_add_u32 s14, s6, s28
	s_addc_u32 s15, s7, 0
	s_lshl_b32 s29, s16, 2
	v_mad_u32_u24 v102, v160, s29, v134
	v_mad_u32_u24 v98, v161, s29, v134
	v_mad_u32_u24 v110, v162, s29, v134
	v_mad_u32_u24 v106, v163, s29, v134
	global_load_dwordx4 v[102:105], v102, s[14:15] nt
	global_load_dwordx4 v[98:101], v98, s[14:15] nt
	global_load_dwordx4 v[110:113], v110, s[14:15] nt
	global_load_dwordx4 v[106:109], v106, s[14:15] nt
.LBB0_1358:
	s_waitcnt vmcnt(28)
	s_mov_b32 s28, 0x42800000
	s_mov_b32 s29, 0x42800000
	v_pk_mul_f32 v[82:83], v[82:83], s[28:29]
	v_pk_mul_f32 v[84:85], v[84:85], s[28:29]
	v_pk_mul_f32 v[86:87], v[86:87], s[28:29]
	v_pk_mul_f32 v[88:89], v[88:89], s[28:29]
	v_pk_mul_f32 v[90:91], v[90:91], s[28:29]
	v_pk_mul_f32 v[92:93], v[92:93], s[28:29]
	v_pk_mul_f32 v[94:95], v[94:95], s[28:29]
	v_pk_mul_f32 v[96:97], v[96:97], s[28:29]
	v_med3_f32 v82, v82, s24, v190
	v_med3_f32 v83, v83, s24, v190
	v_med3_f32 v84, v84, s24, v190
	v_med3_f32 v85, v85, s24, v190
	v_med3_f32 v86, v86, s24, v190
	v_med3_f32 v87, v87, s24, v190
	v_med3_f32 v88, v88, s24, v190
	v_med3_f32 v89, v89, s24, v190
	v_med3_f32 v90, v90, s24, v190
	v_med3_f32 v91, v91, s24, v190
	v_med3_f32 v92, v92, s24, v190
	v_med3_f32 v93, v93, s24, v190
	v_med3_f32 v94, v94, s24, v190
	v_med3_f32 v95, v95, s24, v190
	v_med3_f32 v96, v96, s24, v190
	v_med3_f32 v97, v97, s24, v190
	v_cvt_pk_fp8_f32 v195, v86, v82
	v_cvt_pk_fp8_f32 v195, v94, v90 op_sel:[0,0,1]
	v_cvt_pk_fp8_f32 v196, v87, v83
	v_cvt_pk_fp8_f32 v196, v95, v91 op_sel:[0,0,1]
	v_cvt_pk_fp8_f32 v197, v88, v84
	v_cvt_pk_fp8_f32 v197, v96, v92 op_sel:[0,0,1]
	v_cvt_pk_fp8_f32 v198, v89, v85
	v_cvt_pk_fp8_f32 v198, v97, v93 op_sel:[0,0,1]
	s_and_b64 vcc, exec, s[2:3]
	ds_write2_b32 v191, v195, v196 offset0:8 offset1:41
	ds_write2_b32 v191, v197, v198 offset0:74 offset1:107
	s_cbranch_vccnz .LBB0_1360
	s_mul_i32 s28, s26, s16
	s_add_i32 s28, s28, s0
	s_lshl_b32 s28, s28, 2
	s_add_u32 s14, s6, s28
	s_addc_u32 s15, s7, 0
	s_lshl_b32 s29, s16, 2
	v_mad_u32_u24 v86, v164, s29, v134
	v_mad_u32_u24 v82, v165, s29, v134
	v_mad_u32_u24 v94, v166, s29, v134
	v_mad_u32_u24 v90, v167, s29, v134
	global_load_dwordx4 v[86:89], v86, s[14:15] nt
	global_load_dwordx4 v[82:85], v82, s[14:15] nt
	global_load_dwordx4 v[94:97], v94, s[14:15] nt
	global_load_dwordx4 v[90:93], v90, s[14:15] nt
; #define LAS __attribute__((address_space(3)))
; DI unsigned pk4_fp8(float a, float b, float c, float d) { unsigned p = 0u; p = __builtin_amdgcn_cvt_pk_fp8_f32(f8clamp(a), f8clamp(b), p, false); p = __builtin_amdgcn_cvt_pk_fp8_f32(f8clamp(c), f8clamp(d), p, true); return p; }
; DI float f8clamp(float x) { return __builtin_amdgcn_fmed3f(x, -448.f, 448.f); }
; DI void f8_convert_reload(f32x4 (&v)[4][4], int hb, float sc, LAS unsigned char* scr, bool reload, const F8Tile& dn, int lane) {
;     const int nq = lane & 15, kq = lane >> 4;
; #pragma unroll
;     for (int it = 0; it < 4; ++it) {
; #pragma unroll
;         for (int i = 0; i < 4; ++i) *(LAS unsigned*)(scr + (4 * nq + i) * 132 + hb * 64 + it * 16 + kq * 4) = pk4_fp8(v[it][0][i] * sc, v[it][1][i] * sc, v[it][2][i] * sc, v[it][3][i] * sc);
;         if (reload) {
; #pragma unroll
;             for (int j = 0; j < 4; ++j) v[it][j] = __builtin_nontemporal_load((const f32x4*)(dn.W + (size_t)(dn.k0 + hb * 64 + it * 16 + kq * 4 + j) * dn.N + dn.n0 + 4 * nq)); } }
; }
.LBB0_1360:
	s_waitcnt vmcnt(28)
	s_mov_b32 s28, 0x42800000
	s_mov_b32 s29, 0x42800000
	v_pk_mul_f32 v[66:67], v[66:67], s[28:29]
	v_pk_mul_f32 v[68:69], v[68:69], s[28:29]
	v_pk_mul_f32 v[70:71], v[70:71], s[28:29]
	v_pk_mul_f32 v[72:73], v[72:73], s[28:29]
	v_pk_mul_f32 v[74:75], v[74:75], s[28:29]
	v_pk_mul_f32 v[76:77], v[76:77], s[28:29]
	v_pk_mul_f32 v[78:79], v[78:79], s[28:29]
	v_pk_mul_f32 v[80:81], v[80:81], s[28:29]
	v_med3_f32 v66, v66, s24, v190
	v_med3_f32 v67, v67, s24, v190
	v_med3_f32 v68, v68, s24, v190
	v_med3_f32 v69, v69, s24, v190
	v_med3_f32 v70, v70, s24, v190
	v_med3_f32 v71, v71, s24, v190
	v_med3_f32 v72, v72, s24, v190
	v_med3_f32 v73, v73, s24, v190
	v_med3_f32 v74, v74, s24, v190
	v_med3_f32 v75, v75, s24, v190
	v_med3_f32 v76, v76, s24, v190
	v_med3_f32 v77, v77, s24, v190
	v_med3_f32 v78, v78, s24, v190
	v_med3_f32 v79, v79, s24, v190
	v_med3_f32 v80, v80, s24, v190
	v_med3_f32 v81, v81, s24, v190
	v_cvt_pk_fp8_f32 v195, v70, v66
	v_cvt_pk_fp8_f32 v195, v74, v78 op_sel:[0,0,1]
	v_cvt_pk_fp8_f32 v196, v71, v67
	v_cvt_pk_fp8_f32 v196, v75, v79 op_sel:[0,0,1]
	v_cvt_pk_fp8_f32 v197, v72, v68
	v_cvt_pk_fp8_f32 v197, v76, v80 op_sel:[0,0,1]
	v_cvt_pk_fp8_f32 v198, v73, v69
	v_cvt_pk_fp8_f32 v198, v77, v81 op_sel:[0,0,1]
	s_and_b64 vcc, exec, s[2:3]
	ds_write2_b32 v191, v195, v196 offset0:12 offset1:45
	ds_write2_b32 v191, v197, v198 offset0:78 offset1:111
	s_cbranch_vccnz .LBB0_1362
	s_mul_i32 s28, s26, s16
	s_add_i32 s28, s28, s0
	s_lshl_b32 s28, s28, 2
	s_add_u32 s14, s6, s28
	s_addc_u32 s15, s7, 0
	s_lshl_b32 s29, s16, 2
	v_mad_u32_u24 v70, v168, s29, v134
	v_mad_u32_u24 v66, v169, s29, v134
	v_mad_u32_u24 v74, v171, s29, v134
	v_mad_u32_u24 v78, v172, s29, v134
	global_load_dwordx4 v[70:73], v70, s[14:15] nt
	global_load_dwordx4 v[66:69], v66, s[14:15] nt
	global_load_dwordx4 v[74:77], v74, s[14:15] nt
	global_load_dwordx4 v[78:81], v78, s[14:15] nt
.LBB0_1362:
	s_waitcnt vmcnt(28)
	s_mov_b32 s28, 0x42800000
	s_mov_b32 s29, 0x42800000
	v_pk_mul_f32 v[50:51], v[50:51], s[28:29]
	v_pk_mul_f32 v[52:53], v[52:53], s[28:29]
	v_pk_mul_f32 v[54:55], v[54:55], s[28:29]
	v_pk_mul_f32 v[56:57], v[56:57], s[28:29]
	v_pk_mul_f32 v[58:59], v[58:59], s[28:29]
	v_pk_mul_f32 v[60:61], v[60:61], s[28:29]
	v_pk_mul_f32 v[62:63], v[62:63], s[28:29]
	v_pk_mul_f32 v[64:65], v[64:65], s[28:29]
	v_med3_f32 v50, v50, s24, v190
	v_med3_f32 v51, v51, s24, v190
	v_med3_f32 v52, v52, s24, v190
	v_med3_f32 v53, v53, s24, v190
	v_med3_f32 v54, v54, s24, v190
	v_med3_f32 v55, v55, s24, v190
	v_med3_f32 v56, v56, s24, v190
	v_med3_f32 v57, v57, s24, v190
	v_med3_f32 v58, v58, s24, v190
	v_med3_f32 v59, v59, s24, v190
	v_med3_f32 v60, v60, s24, v190
	v_med3_f32 v61, v61, s24, v190
	v_med3_f32 v62, v62, s24, v190
	v_med3_f32 v63, v63, s24, v190
	v_med3_f32 v64, v64, s24, v190
	v_med3_f32 v65, v65, s24, v190
	v_cvt_pk_fp8_f32 v195, v54, v50
	v_cvt_pk_fp8_f32 v195, v62, v58 op_sel:[0,0,1]
	v_cvt_pk_fp8_f32 v196, v55, v51
	v_cvt_pk_fp8_f32 v196, v63, v59 op_sel:[0,0,1]
	v_cvt_pk_fp8_f32 v197, v56, v52
	v_cvt_pk_fp8_f32 v197, v64, v60 op_sel:[0,0,1]
	v_cvt_pk_fp8_f32 v198, v57, v53
	v_cvt_pk_fp8_f32 v198, v65, v61 op_sel:[0,0,1]
	s_and_b64 vcc, exec, s[2:3]
	ds_write2_b32 v191, v195, v196 offset0:16 offset1:49
	ds_write2_b32 v191, v197, v198 offset0:82 offset1:115
	s_cbranch_vccnz .LBB0_1364
	s_mul_i32 s28, s26, s16
	s_add_i32 s28, s28, s0
	s_lshl_b32 s28, s28, 2
	s_add_u32 s14, s6, s28
	s_addc_u32 s15, s7, 0
	s_lshl_b32 s29, s16, 2
	v_mad_u32_u24 v54, v173, s29, v134
	v_mad_u32_u24 v50, v174, s29, v134
	v_mad_u32_u24 v62, v175, s29, v134
	v_mad_u32_u24 v58, v176, s29, v134
	global_load_dwordx4 v[54:57], v54, s[14:15] nt
	global_load_dwordx4 v[50:53], v50, s[14:15] nt
	global_load_dwordx4 v[62:65], v62, s[14:15] nt
	global_load_dwordx4 v[58:61], v58, s[14:15] nt
; #define LAS __attribute__((address_space(3)))
; DI unsigned pk4_fp8(float a, float b, float c, float d) { unsigned p = 0u; p = __builtin_amdgcn_cvt_pk_fp8_f32(f8clamp(a), f8clamp(b), p, false); p = __builtin_amdgcn_cvt_pk_fp8_f32(f8clamp(c), f8clamp(d), p, true); return p; }
; DI void f8_convert_reload(f32x4 (&v)[4][4], int hb, float sc, LAS unsigned char* scr, bool reload, const F8Tile& dn, int lane) {
;     ...
;     for (int it = 0; it < 4; ++it) {
; #pragma unroll
;         for (int i = 0; i < 4; ++i) *(LAS unsigned*)(scr + (4 * nq + i) * 132 + hb * 64 + it * 16 + kq * 4) = pk4_fp8(v[it][0][i] * sc, v[it][1][i] * sc, v[it][2][i] * sc, v[it][3][i] * sc);
.LBB0_1364:
	s_waitcnt vmcnt(28)
	s_mov_b32 s28, 0x42800000
	s_mov_b32 s29, 0x42800000
	v_pk_mul_f32 v[34:35], v[34:35], s[28:29]
	v_pk_mul_f32 v[36:37], v[36:37], s[28:29]
	v_pk_mul_f32 v[38:39], v[38:39], s[28:29]
	v_pk_mul_f32 v[40:41], v[40:41], s[28:29]
	v_pk_mul_f32 v[42:43], v[42:43], s[28:29]
	v_pk_mul_f32 v[44:45], v[44:45], s[28:29]
	v_pk_mul_f32 v[46:47], v[46:47], s[28:29]
	v_pk_mul_f32 v[48:49], v[48:49], s[28:29]
	v_med3_f32 v34, v34, s24, v190
	v_med3_f32 v35, v35, s24, v190
	v_med3_f32 v36, v36, s24, v190
	v_med3_f32 v37, v37, s24, v190
	v_med3_f32 v38, v38, s24, v190
	v_med3_f32 v39, v39, s24, v190
	v_med3_f32 v40, v40, s24, v190
	v_med3_f32 v41, v41, s24, v190
	v_med3_f32 v42, v42, s24, v190
	v_med3_f32 v43, v43, s24, v190
	v_med3_f32 v44, v44, s24, v190
	v_med3_f32 v45, v45, s24, v190
	v_med3_f32 v46, v46, s24, v190
	v_med3_f32 v47, v47, s24, v190
	v_med3_f32 v48, v48, s24, v190
	v_med3_f32 v49, v49, s24, v190
	v_cvt_pk_fp8_f32 v195, v38, v34
	v_cvt_pk_fp8_f32 v195, v46, v42 op_sel:[0,0,1]
	v_cvt_pk_fp8_f32 v196, v39, v35
	v_cvt_pk_fp8_f32 v196, v47, v43 op_sel:[0,0,1]
	v_cvt_pk_fp8_f32 v197, v40, v36
	v_cvt_pk_fp8_f32 v197, v48, v44 op_sel:[0,0,1]
	v_cvt_pk_fp8_f32 v198, v41, v37
	v_cvt_pk_fp8_f32 v198, v49, v45 op_sel:[0,0,1]
	s_and_b64 vcc, exec, s[2:3]
	ds_write2_b32 v191, v195, v196 offset0:20 offset1:53
	ds_write2_b32 v191, v197, v198 offset0:86 offset1:119
	s_cbranch_vccnz .LBB0_1366
	s_mul_i32 s28, s26, s16
	s_add_i32 s28, s28, s0
	s_lshl_b32 s28, s28, 2
	s_add_u32 s14, s6, s28
	s_addc_u32 s15, s7, 0
	s_lshl_b32 s29, s16, 2
	v_mad_u32_u24 v38, v177, s29, v134
	v_mad_u32_u24 v34, v178, s29, v134
	v_mad_u32_u24 v46, v179, s29, v134
	v_mad_u32_u24 v42, v180, s29, v134
	global_load_dwordx4 v[38:41], v38, s[14:15] nt
	global_load_dwordx4 v[34:37], v34, s[14:15] nt
	global_load_dwordx4 v[46:49], v46, s[14:15] nt
	global_load_dwordx4 v[42:45], v42, s[14:15] nt
.LBB0_1366:
	s_waitcnt vmcnt(28)
	s_mov_b32 s28, 0x42800000
	s_mov_b32 s29, 0x42800000
	v_pk_mul_f32 v[18:19], v[18:19], s[28:29]
	v_pk_mul_f32 v[20:21], v[20:21], s[28:29]
	v_pk_mul_f32 v[22:23], v[22:23], s[28:29]
	v_pk_mul_f32 v[24:25], v[24:25], s[28:29]
	v_pk_mul_f32 v[26:27], v[26:27], s[28:29]
	v_pk_mul_f32 v[28:29], v[28:29], s[28:29]
	v_pk_mul_f32 v[30:31], v[30:31], s[28:29]
	v_pk_mul_f32 v[32:33], v[32:33], s[28:29]
	v_med3_f32 v18, v18, s24, v190
	v_med3_f32 v19, v19, s24, v190
	v_med3_f32 v20, v20, s24, v190
	v_med3_f32 v21, v21, s24, v190
	v_med3_f32 v22, v22, s24, v190
	v_med3_f32 v23, v23, s24, v190
	v_med3_f32 v24, v24, s24, v190
	v_med3_f32 v25, v25, s24, v190
	v_med3_f32 v26, v26, s24, v190
	v_med3_f32 v27, v27, s24, v190
	v_med3_f32 v28, v28, s24, v190
	v_med3_f32 v29, v29, s24, v190
	v_med3_f32 v30, v30, s24, v190
	v_med3_f32 v31, v31, s24, v190
	v_med3_f32 v32, v32, s24, v190
	v_med3_f32 v33, v33, s24, v190
	v_cvt_pk_fp8_f32 v195, v22, v18
	v_cvt_pk_fp8_f32 v195, v30, v26 op_sel:[0,0,1]
	v_cvt_pk_fp8_f32 v196, v23, v19
	v_cvt_pk_fp8_f32 v196, v31, v27 op_sel:[0,0,1]
	v_cvt_pk_fp8_f32 v197, v24, v20
	v_cvt_pk_fp8_f32 v197, v32, v28 op_sel:[0,0,1]
	v_cvt_pk_fp8_f32 v198, v25, v21
	v_cvt_pk_fp8_f32 v198, v33, v29 op_sel:[0,0,1]
	s_and_b64 vcc, exec, s[2:3]
	ds_write2_b32 v191, v195, v196 offset0:24 offset1:57
	ds_write2_b32 v191, v197, v198 offset0:90 offset1:123
	s_cbranch_vccnz .LBB0_1368
	s_mul_i32 s28, s26, s16
	s_add_i32 s28, s28, s0
	s_lshl_b32 s28, s28, 2
	s_add_u32 s14, s6, s28
	s_addc_u32 s15, s7, 0
	s_lshl_b32 s29, s16, 2
	v_mad_u32_u24 v22, v181, s29, v134
	v_mad_u32_u24 v18, v182, s29, v134
	v_mad_u32_u24 v30, v183, s29, v134
	v_mad_u32_u24 v26, v184, s29, v134
	global_load_dwordx4 v[22:25], v22, s[14:15] nt
	global_load_dwordx4 v[18:21], v18, s[14:15] nt
	global_load_dwordx4 v[30:33], v30, s[14:15] nt
	global_load_dwordx4 v[26:29], v26, s[14:15] nt
.LBB0_1368:
	s_waitcnt vmcnt(28)
	s_mov_b32 s14, 0x42800000
	s_mov_b32 s15, 0x42800000
	v_pk_mul_f32 v[2:3], v[2:3], s[14:15]
	v_pk_mul_f32 v[4:5], v[4:5], s[14:15]
	v_pk_mul_f32 v[6:7], v[6:7], s[14:15]
	v_pk_mul_f32 v[8:9], v[8:9], s[14:15]
	v_pk_mul_f32 v[10:11], v[10:11], s[14:15]
	v_pk_mul_f32 v[12:13], v[12:13], s[14:15]
	v_pk_mul_f32 v[14:15], v[14:15], s[14:15]
	v_pk_mul_f32 v[16:17], v[16:17], s[14:15]
	v_med3_f32 v2, v2, s24, v190
	v_med3_f32 v3, v3, s24, v190
	v_med3_f32 v4, v4, s24, v190
	v_med3_f32 v5, v5, s24, v190
	v_med3_f32 v6, v6, s24, v190
	v_med3_f32 v7, v7, s24, v190
	v_med3_f32 v8, v8, s24, v190
	v_med3_f32 v9, v9, s24, v190
	v_med3_f32 v10, v10, s24, v190
	v_med3_f32 v11, v11, s24, v190
	v_med3_f32 v12, v12, s24, v190
	v_med3_f32 v13, v13, s24, v190
	v_med3_f32 v14, v14, s24, v190
	v_med3_f32 v15, v15, s24, v190
	v_med3_f32 v16, v16, s24, v190
	v_med3_f32 v17, v17, s24, v190
	v_cvt_pk_fp8_f32 v195, v6, v2
	v_cvt_pk_fp8_f32 v195, v14, v10 op_sel:[0,0,1]
	v_cvt_pk_fp8_f32 v196, v7, v3
	v_cvt_pk_fp8_f32 v196, v15, v11 op_sel:[0,0,1]
	v_cvt_pk_fp8_f32 v197, v8, v4
	v_cvt_pk_fp8_f32 v197, v16, v12 op_sel:[0,0,1]
	v_cvt_pk_fp8_f32 v198, v9, v5
	v_cvt_pk_fp8_f32 v198, v17, v13 op_sel:[0,0,1]
	s_and_b64 vcc, exec, s[2:3]
	ds_write2_b32 v191, v195, v196 offset0:28 offset1:61
	ds_write2_b32 v191, v197, v198 offset0:94 offset1:127
	s_cbranch_vccnz .LBB0_1346
	s_mul_i32 s14, s26, s16
	s_add_i32 s14, s14, s0
	s_lshl_b32 s14, s14, 2
	s_add_u32 s2, s6, s14
	s_addc_u32 s3, s7, 0
	s_lshl_b32 s15, s16, 2
	v_mad_u32_u24 v6, v185, s15, v134
	v_mad_u32_u24 v2, v186, s15, v134
	v_mad_u32_u24 v14, v187, s15, v134
	v_mad_u32_u24 v10, v188, s15, v134
	global_load_dwordx4 v[6:9], v6, s[2:3] nt
	global_load_dwordx4 v[2:5], v2, s[2:3] nt
	global_load_dwordx4 v[14:17], v14, s[2:3] nt
	global_load_dwordx4 v[10:13], v10, s[2:3] nt
	s_branch .LBB0_1346
